# baseline (speedup 1.0000x reference)
_Z11main_kernelPKDv8_DF16bS1_PKfS3_S3_PKiPKtS3_S3_Pf:
	s_lshl_b32 s14, s2, 5
	s_load_dwordx4 s[4:7], s[0:1], 0x0
	s_load_dwordx2 s[36:37], s[0:1], 0x10
	s_load_dwordx4 s[8:11], s[0:1], 0x28
	s_and_b32 s3, s14, 0xe0
	s_lshr_b32 s33, s2, 3
	s_or_b32 s15, s3, s33
	v_lshrrev_b32_e32 v73, 6, v0
	s_lshl_b32 s34, s15, 3
	v_or_b32_e32 v54, s34, v73
	v_mov_b32_e32 v55, 0
	v_and_b32_e32 v1, 63, v0
	v_lshlrev_b64 v[2:3], 7, v[54:55]
	s_waitcnt lgkmcnt(0)
	v_mov_b32_e32 v205, 0
	global_load_dword v204, v205, s[6:7]
	v_lshl_add_u64 v[2:3], s[10:11], 0, v[2:3]
	v_lshlrev_b32_e32 v4, 1, v1
	v_mov_b32_e32 v5, v55
	v_lshl_add_u64 v[2:3], v[2:3], 0, v[4:5]
	global_load_ushort v72, v[2:3], off
	v_and_b32_e32 v2, 7, v0
	v_bfe_u32 v74, v0, 4, 2
	v_lshlrev_b32_e32 v2, 4, v2
	s_mov_b32 s13, 0
	s_lshl_b32 s2, s15, 1
	s_lshl_b32 s12, s15, 2
	v_lshl_or_b32 v2, v74, 7, v2
	v_mov_b32_e32 v3, v55
	s_and_b32 s10, s2, 0x3ffffffc
	v_lshl_add_u64 v[58:59], s[4:5], 0, v[2:3]
	s_lshl_b64 s[2:3], s[12:13], 9
	v_lshl_add_u64 v[2:3], v[58:59], 0, s[2:3]
	s_or_b32 s2, s12, 1
	s_mov_b32 s3, s13
	s_lshl_b64 s[2:3], s[2:3], 9
	v_lshl_add_u64 v[4:5], v[58:59], 0, s[2:3]
	s_or_b32 s2, s12, 2
	s_mov_b32 s3, s13
	s_lshl_b64 s[2:3], s[2:3], 9
	global_load_dwordx4 v[22:25], v[2:3], off
	global_load_dwordx4 v[50:53], v[4:5], off
	v_lshl_add_u64 v[2:3], v[58:59], 0, s[2:3]
	s_or_b32 s2, s12, 3
	s_mov_b32 s3, s13
	s_lshl_b64 s[2:3], s[2:3], 9
	v_lshl_add_u64 v[4:5], v[58:59], 0, s[2:3]
	s_and_b32 s2, s14, 0x700
	s_add_i32 s5, s33, 1
	s_lshl_b32 s14, s2, 4
	s_lshl_b32 s2, s5, 8
	s_and_b32 s2, s2, 0x700
	s_add_i32 s38, s33, 2
	s_lshl_b32 s16, s2, 4
	s_lshl_b32 s2, s38, 8
	s_and_b32 s2, s2, 0x700
	s_add_i32 s39, s33, 3
	s_lshl_b32 s18, s2, 4
	s_lshl_b32 s2, s39, 8
	s_and_b32 s44, s15, 0x1fffff80
	v_lshlrev_b32_e32 v75, 3, v73
	s_and_b32 s2, s2, 0x700
	s_add_i32 s40, s33, 4
	global_load_dwordx4 v[60:63], v[2:3], off
	global_load_dwordx4 v[64:67], v[4:5], off
	v_or_b32_e32 v2, s44, v75
	v_mov_b32_e32 v3, v55
	s_lshl_b32 s20, s2, 4
	s_lshl_b32 s2, s40, 8
	v_lshlrev_b64 v[2:3], 12, v[2:3]
	s_and_b32 s2, s2, 0x700
	s_add_i32 s41, s33, 5
	v_lshl_add_u64 v[2:3], s[6:7], 0, v[2:3]
	v_lshlrev_b32_e32 v56, 4, v1
	v_mov_b32_e32 v57, v55
	s_lshl_b32 s22, s2, 4
	s_lshl_b32 s2, s41, 8
	v_lshl_add_u64 v[2:3], v[2:3], 0, v[56:57]
	s_mov_b32 s15, s13
	s_and_b32 s2, s2, 0x700
	s_add_i32 s42, s33, 6
	v_lshl_add_u64 v[4:5], v[2:3], 0, s[14:15]
	s_mov_b32 s17, s13
	s_lshl_b32 s24, s2, 4
	s_lshl_b32 s2, s42, 8
	global_load_dwordx4 v[18:21], v[4:5], off
	global_load_dwordx4 v[26:29], v[4:5], off offset:1024
	global_load_dwordx4 v[30:33], v[4:5], off offset:2048
	global_load_dwordx4 v[34:37], v[4:5], off offset:3072
	v_lshl_add_u64 v[4:5], v[2:3], 0, s[16:17]
	s_mov_b32 s19, s13
	s_and_b32 s2, s2, 0x700
	s_add_i32 s43, s33, 7
	global_load_dwordx4 v[38:41], v[4:5], off
	global_load_dwordx4 v[42:45], v[4:5], off offset:1024
	global_load_dwordx4 v[68:71], v[4:5], off offset:2048
	global_load_dwordx4 v[76:79], v[4:5], off offset:3072
	v_lshl_add_u64 v[4:5], v[2:3], 0, s[18:19]
	s_mov_b32 s21, s13
	s_lshl_b32 s26, s2, 4
	s_lshl_b32 s2, s43, 8
	global_load_dwordx4 v[80:83], v[4:5], off
	global_load_dwordx4 v[84:87], v[4:5], off offset:1024
	global_load_dwordx4 v[88:91], v[4:5], off offset:2048
	global_load_dwordx4 v[92:95], v[4:5], off offset:3072
	v_lshl_add_u64 v[4:5], v[2:3], 0, s[20:21]
	s_mov_b32 s23, s13
	s_and_b32 s2, s2, 0x700
	s_and_b32 s30, s34, 0x7ffffc00
	s_mov_b32 s31, s13
	global_load_dwordx4 v[96:99], v[4:5], off
	global_load_dwordx4 v[100:103], v[4:5], off offset:1024
	global_load_dwordx4 v[104:107], v[4:5], off offset:2048
	global_load_dwordx4 v[108:111], v[4:5], off offset:3072
	v_lshl_add_u64 v[4:5], v[2:3], 0, s[22:23]
	s_mov_b32 s25, s13
	s_lshl_b32 s28, s2, 4
	s_lshl_b64 s[2:3], s[30:31], 2
	global_load_dwordx4 v[112:115], v[4:5], off
	global_load_dwordx4 v[116:119], v[4:5], off offset:1024
	global_load_dwordx4 v[120:123], v[4:5], off offset:2048
	global_load_dwordx4 v[124:127], v[4:5], off offset:3072
	v_lshl_add_u64 v[4:5], v[2:3], 0, s[24:25]
	s_mov_b32 s27, s13
	s_mov_b32 s29, s13
	s_add_u32 s2, s36, s2
	global_load_dwordx4 v[128:131], v[4:5], off
	global_load_dwordx4 v[132:135], v[4:5], off offset:1024
	global_load_dwordx4 v[136:139], v[4:5], off offset:2048
	global_load_dwordx4 v[140:143], v[4:5], off offset:3072
	v_lshl_add_u64 v[4:5], v[2:3], 0, s[26:27]
	v_lshl_add_u64 v[2:3], v[2:3], 0, s[28:29]
	s_addc_u32 s3, s37, s3
	global_load_dwordx4 v[144:147], v[4:5], off
	global_load_dwordx4 v[148:151], v[4:5], off offset:1024
	global_load_dwordx4 v[152:155], v[4:5], off offset:2048
	global_load_dwordx4 v[156:159], v[4:5], off offset:3072
	global_load_dwordx4 v[160:163], v[2:3], off
	global_load_dwordx4 v[164:167], v[2:3], off offset:1024
	global_load_dwordx4 v[168:171], v[2:3], off offset:2048
	global_load_dwordx4 v[172:175], v[2:3], off offset:3072
	global_load_dwordx4 v[14:17], v56, s[2:3]
	global_load_dwordx4 v[10:13], v56, s[2:3] offset:1024
	global_load_dwordx4 v[6:9], v56, s[2:3] offset:2048
	s_nop 0
	global_load_dwordx4 v[2:5], v56, s[2:3] offset:3072
	s_load_dwordx2 s[2:3], s[0:1], 0x40
	s_load_dword s15, s[8:9], s10 offset:0x0
	v_lshlrev_b32_e32 v1, 2, v1
	s_waitcnt lgkmcnt(0)
	s_load_dword s4, s[2:3], 0x0
	s_waitcnt vmcnt(35)
	v_mfma_f32_16x16x32_bf16 v[18:21], v[22:25], v[18:21], 0
	s_cmp_lt_i32 s15, 3
	s_cselect_b64 s[2:3], -1, 0
	s_mov_b64 s[8:9], -1
	s_waitcnt vmcnt(34)
	v_mfma_f32_16x16x32_bf16 v[18:21], v[50:53], v[26:29], v[18:21]
	s_and_b64 vcc, exec, s[2:3]
	s_waitcnt vmcnt(33)
	v_mfma_f32_16x16x32_bf16 v[18:21], v[60:63], v[30:33], v[18:21]
	s_waitcnt vmcnt(32)
	v_mfma_f32_16x16x32_bf16 v[46:49], v[64:67], v[34:37], v[18:21]
	s_waitcnt vmcnt(31)
	v_mfma_f32_16x16x32_bf16 v[18:21], v[22:25], v[38:41], 0
	s_waitcnt vmcnt(30)
	v_mfma_f32_16x16x32_bf16 v[18:21], v[50:53], v[42:45], v[18:21]
	s_waitcnt vmcnt(29)
	v_mfma_f32_16x16x32_bf16 v[18:21], v[60:63], v[68:71], v[18:21]
	s_waitcnt vmcnt(28)
	v_mfma_f32_16x16x32_bf16 v[42:45], v[64:67], v[76:79], v[18:21]
	s_waitcnt vmcnt(27)
	v_mfma_f32_16x16x32_bf16 v[18:21], v[22:25], v[80:83], 0
	s_waitcnt vmcnt(26)
	v_mfma_f32_16x16x32_bf16 v[18:21], v[50:53], v[84:87], v[18:21]
	s_waitcnt vmcnt(25)
	v_mfma_f32_16x16x32_bf16 v[18:21], v[60:63], v[88:91], v[18:21]
	s_waitcnt vmcnt(24)
	v_mfma_f32_16x16x32_bf16 v[38:41], v[64:67], v[92:95], v[18:21]
	s_waitcnt vmcnt(23)
	v_mfma_f32_16x16x32_bf16 v[18:21], v[22:25], v[96:99], 0
	s_waitcnt vmcnt(22)
	v_mfma_f32_16x16x32_bf16 v[18:21], v[50:53], v[100:103], v[18:21]
	s_waitcnt vmcnt(21)
	v_mfma_f32_16x16x32_bf16 v[18:21], v[60:63], v[104:107], v[18:21]
	s_waitcnt vmcnt(20)
	v_mfma_f32_16x16x32_bf16 v[34:37], v[64:67], v[108:111], v[18:21]
	s_waitcnt vmcnt(19)
	v_mfma_f32_16x16x32_bf16 v[18:21], v[22:25], v[112:115], 0
	s_waitcnt vmcnt(18)
	v_mfma_f32_16x16x32_bf16 v[18:21], v[50:53], v[116:119], v[18:21]
	s_waitcnt vmcnt(17)
	v_mfma_f32_16x16x32_bf16 v[18:21], v[60:63], v[120:123], v[18:21]
	s_waitcnt vmcnt(16)
	v_mfma_f32_16x16x32_bf16 v[30:33], v[64:67], v[124:127], v[18:21]
	s_waitcnt vmcnt(15)
	v_mfma_f32_16x16x32_bf16 v[18:21], v[22:25], v[128:131], 0
	s_waitcnt vmcnt(14)
	v_mfma_f32_16x16x32_bf16 v[18:21], v[50:53], v[132:135], v[18:21]
	s_waitcnt vmcnt(13)
	v_mfma_f32_16x16x32_bf16 v[18:21], v[60:63], v[136:139], v[18:21]
	s_waitcnt vmcnt(12)
	v_mfma_f32_16x16x32_bf16 v[26:29], v[64:67], v[140:143], v[18:21]
	s_waitcnt vmcnt(11)
	v_mfma_f32_16x16x32_bf16 v[18:21], v[22:25], v[144:147], 0
	s_waitcnt vmcnt(7)
	v_mfma_f32_16x16x32_bf16 v[22:25], v[22:25], v[160:163], 0
	v_mfma_f32_16x16x32_bf16 v[18:21], v[50:53], v[148:151], v[18:21]
	s_waitcnt vmcnt(6)
	v_mfma_f32_16x16x32_bf16 v[22:25], v[50:53], v[164:167], v[22:25]
	v_mfma_f32_16x16x32_bf16 v[18:21], v[60:63], v[152:155], v[18:21]
	s_waitcnt vmcnt(5)
	v_mfma_f32_16x16x32_bf16 v[22:25], v[60:63], v[168:171], v[22:25]
	v_mfma_f32_16x16x32_bf16 v[18:21], v[64:67], v[156:159], v[18:21]
	s_waitcnt vmcnt(4)
	v_mfma_f32_16x16x32_bf16 v[22:25], v[64:67], v[172:175], v[22:25]
	s_cbranch_vccz .LBB1_5
	s_load_dwordx2 s[0:1], s[0:1], 0x48
	s_and_b64 vcc, exec, s[8:9]
	s_cbranch_vccz .LBB1_4
	s_cmp_lg_u32 s15, 2
	s_cbranch_scc0 .LBB1_14

	.amdhsa_kernel _Z11main_kernelPKDv8_DF16bS1_PKfS3_S3_PKiPKtS3_S3_Pf
		.amdhsa_group_segment_fixed_size 70400
		.amdhsa_private_segment_fixed_size 0
		.amdhsa_kernarg_size 80
		.amdhsa_user_sgpr_count 2
		.amdhsa_user_sgpr_dispatch_ptr 0
		.amdhsa_user_sgpr_queue_ptr 0
		.amdhsa_user_sgpr_kernarg_segment_ptr 1
		.amdhsa_user_sgpr_dispatch_id 0
		.amdhsa_user_sgpr_kernarg_preload_length 0
		.amdhsa_user_sgpr_kernarg_preload_offset 0
		.amdhsa_user_sgpr_private_segment_size 0
		.amdhsa_uses_dynamic_stack 0
		.amdhsa_enable_private_segment 0
		.amdhsa_system_sgpr_workgroup_id_x 1
		.amdhsa_system_sgpr_workgroup_id_y 0
		.amdhsa_system_sgpr_workgroup_id_z 0
		.amdhsa_system_sgpr_workgroup_info 0
		.amdhsa_system_vgpr_workitem_id 0
		.amdhsa_next_free_vgpr 208
		.amdhsa_next_free_sgpr 96
		.amdhsa_accum_offset 208
		.amdhsa_reserve_vcc 1
		.amdhsa_float_round_mode_32 0
		.amdhsa_float_round_mode_16_64 0
		.amdhsa_float_denorm_mode_32 3
		.amdhsa_float_denorm_mode_16_64 3
		.amdhsa_dx10_clamp 1
		.amdhsa_ieee_mode 1
		.amdhsa_fp16_overflow 0
		.amdhsa_tg_split 0
		.amdhsa_exception_fp_ieee_invalid_op 0
		.amdhsa_exception_fp_denorm_src 0
		.amdhsa_exception_fp_ieee_div_zero 0
		.amdhsa_exception_fp_ieee_overflow 0
		.amdhsa_exception_fp_ieee_underflow 0
		.amdhsa_exception_fp_ieee_inexact 0
		.amdhsa_exception_int_div_zero 0
	.end_amdhsa_kernel

amdhsa.kernels:
  - .agpr_count:     0
    .args:
      - .actual_access:  read_only
        .address_space:  global
        .offset:         0
        .size:           8
        .value_kind:     global_buffer
      - .actual_access:  read_only
        .address_space:  global
        .offset:         8
        .size:           8
        .value_kind:     global_buffer
      - .actual_access:  read_only
        .address_space:  global
        .offset:         16
        .size:           8
        .value_kind:     global_buffer
      - .actual_access:  read_only
        .address_space:  global
        .offset:         24
        .size:           8
        .value_kind:     global_buffer
      - .actual_access:  read_only
        .address_space:  global
        .offset:         32
        .size:           8
        .value_kind:     global_buffer
      - .actual_access:  read_only
        .address_space:  global
        .offset:         40
        .size:           8
        .value_kind:     global_buffer
      - .actual_access:  read_only
        .address_space:  global
        .offset:         48
        .size:           8
        .value_kind:     global_buffer
      - .actual_access:  read_only
        .address_space:  global
        .offset:         56
        .size:           8
        .value_kind:     global_buffer
      - .actual_access:  read_only
        .address_space:  global
        .offset:         64
        .size:           8
        .value_kind:     global_buffer
      - .actual_access:  read_only
        .address_space:  global
        .offset:         72
        .size:           8
        .value_kind:     global_buffer
      - .actual_access:  write_only
        .address_space:  global
        .offset:         80
        .size:           8
        .value_kind:     global_buffer
      - .actual_access:  write_only
        .address_space:  global
        .offset:         88
        .size:           8
        .value_kind:     global_buffer
      - .actual_access:  write_only
        .address_space:  global
        .offset:         96
        .size:           8
        .value_kind:     global_buffer
      - .actual_access:  write_only
        .address_space:  global
        .offset:         104
        .size:           8
        .value_kind:     global_buffer
      - .actual_access:  write_only
        .address_space:  global
        .offset:         112
        .size:           8
        .value_kind:     global_buffer
      - .actual_access:  write_only
        .address_space:  global
        .offset:         120
        .size:           8
        .value_kind:     global_buffer
      - .actual_access:  write_only
        .address_space:  global
        .offset:         128
        .size:           8
        .value_kind:     global_buffer
    .group_segment_fixed_size: 121344
    .kernarg_segment_align: 8
    .kernarg_segment_size: 136
    .language:       OpenCL C
    .language_version:
      - 2
      - 0
    .max_flat_workgroup_size: 512
    .name:           _Z11prep_kernelPKfS0_S0_S0_S0_S0_S0_S0_S0_PKiPDv8_DF16bS4_PfS5_S5_PiPt
    .private_segment_fixed_size: 0
    .sgpr_count:     31
    .sgpr_spill_count: 0
    .symbol:         _Z11prep_kernelPKfS0_S0_S0_S0_S0_S0_S0_S0_PKiPDv8_DF16bS4_PfS5_S5_PiPt.kd
    .uniform_work_group_size: 1
    .uses_dynamic_stack: false
    .vgpr_count:     164
    .vgpr_spill_count: 0
    .wavefront_size: 64
  - .agpr_count:     0
    .args:
      - .actual_access:  read_only
        .address_space:  global
        .offset:         0
        .size:           8
        .value_kind:     global_buffer
      - .actual_access:  read_only
        .address_space:  global
        .offset:         8
        .size:           8
        .value_kind:     global_buffer
      - .actual_access:  read_only
        .address_space:  global
        .offset:         16
        .size:           8
        .value_kind:     global_buffer
      - .actual_access:  read_only
        .address_space:  global
        .offset:         24
        .size:           8
        .value_kind:     global_buffer
      - .actual_access:  read_only
        .address_space:  global
        .offset:         32
        .size:           8
        .value_kind:     global_buffer
      - .actual_access:  read_only
        .address_space:  global
        .offset:         40
        .size:           8
        .value_kind:     global_buffer
      - .actual_access:  read_only
        .address_space:  global
        .offset:         48
        .size:           8
        .value_kind:     global_buffer
      - .actual_access:  read_only
        .address_space:  global
        .offset:         56
        .size:           8
        .value_kind:     global_buffer
      - .actual_access:  read_only
        .address_space:  global
        .offset:         64
        .size:           8
        .value_kind:     global_buffer
      - .actual_access:  write_only
        .address_space:  global
        .offset:         72
        .size:           8
        .value_kind:     global_buffer
    .group_segment_fixed_size: 70400
    .kernarg_segment_align: 8
    .kernarg_segment_size: 80
    .language:       OpenCL C
    .language_version:
      - 2
      - 0
    .max_flat_workgroup_size: 512
    .name:           _Z11main_kernelPKDv8_DF16bS1_PKfS3_S3_PKiPKtS3_S3_Pf
    .private_segment_fixed_size: 0
    .sgpr_count:     54
    .sgpr_spill_count: 0
    .symbol:         _Z11main_kernelPKDv8_DF16bS1_PKfS3_S3_PKiPKtS3_S3_Pf.kd
    .uniform_work_group_size: 1
    .uses_dynamic_stack: false
    .vgpr_count:     208
    .vgpr_spill_count: 0
    .wavefront_size: 64
